# plus: up-projection epilogue 1/sqrt via v_rsq_f32 instead of the IEEE sqrt+div expansion
# baseline (speedup 1.0000x reference)
.LBB0_400:
	s_lshl_b32 s48, s8, 8
	s_cmp_lg_u32 s58, 0
	v_mbcnt_lo_u32_b32 v112, -1, 0
	v_mbcnt_hi_u32_b32 v112, -1, v112
	s_cselect_b64 s[62:63], -1, 0
	v_and_b32_e32 v237, 15, v112
	s_cmp_eq_u32 s58, 0
	v_or_b32_e32 v231, s85, v237
	s_cselect_b32 s6, 0, 32
	v_add_u32_e32 v232, s48, v231
	s_add_u32 s16, s77, s6
	v_ashrrev_i32_e32 v233, 31, v232
	s_addc_u32 s17, s78, 0
	v_lshlrev_b64 v[114:115], 6, v[232:233]
	v_lshl_add_u64 v[118:119], s[16:17], 0, v[114:115]
	global_load_dwordx4 v[114:117], v[118:119], off
	global_load_dwordx4 v[128:131], v[118:119], off offset:16
	v_mul_f32_e32 v118, v157, v157
	v_mul_f32_e32 v119, v159, v159
	v_mul_f32_e32 v132, v153, v153
	v_mul_f32_e32 v133, v155, v155
	v_fmac_f32_e32 v118, v156, v156
	v_fmac_f32_e32 v119, v158, v158
	v_fmac_f32_e32 v132, v152, v152
	v_fmac_f32_e32 v133, v154, v154
	v_add_f32_e32 v118, v118, v119
	v_ashrrev_i32_e32 v135, 2, v112
	v_cndmask_b32_e64 v134, 0, 1, s[44:45]
	v_and_b32_e32 v208, -4, v135
	s_mov_b64 s[10:11], -1
	v_cmp_ne_u32_e64 s[6:7], 1, v134
	v_ashrrev_i32_e32 v209, 31, v208
	s_waitcnt vmcnt(1)
	v_add_f32_e32 v114, v114, v115
	v_add_f32_e32 v115, v116, v117
	s_waitcnt vmcnt(0)
	v_add_f32_e32 v116, v128, v129
	v_add_f32_e32 v117, v130, v131
	v_add_f32_e32 v114, v114, v115
	v_add_f32_e32 v115, v116, v117
	v_add_f32_e32 v114, v114, v115
	v_fmamk_f32 v114, v114, 0x3b000000, v213
	v_rsq_f32_e32 v236, v114
	v_add_f32_e32 v114, v132, v133
	v_add_f32_e32 v114, v118, v114
	s_and_b64 s[8:9], exec, s[62:63]
	v_mul_f32_e32 v115, v236, v236
	s_mov_b64 vcc, s[8:9]
	s_cbranch_vccz .LBB0_404
	s_and_b64 vcc, exec, s[6:7]
	v_mul_f32_e32 v113, v114, v115
	s_cbranch_vccnz .LBB0_403
	v_mov_b64_e32 v[116:117], s[50:51]
	v_mad_i64_i32 v[116:117], s[8:9], v232, s65, v[116:117]
	v_lshl_add_u64 v[116:117], v[208:209], 1, v[116:117]
	global_load_dwordx2 v[118:119], v[116:117], off offset:2080
	s_nop 0
	global_load_dwordx2 v[116:117], v[116:117], off offset:2048
	s_waitcnt vmcnt(1)
	v_lshlrev_b32_e32 v129, 16, v118
	v_and_b32_e32 v131, 0xffff0000, v118
	s_waitcnt vmcnt(0)
	v_and_b32_e32 v130, 0xffff0000, v116
	v_lshlrev_b32_e32 v133, 16, v119
	v_and_b32_e32 v119, 0xffff0000, v119
	v_and_b32_e32 v118, 0xffff0000, v117
	v_lshlrev_b32_e32 v128, 16, v116
	v_lshlrev_b32_e32 v132, 16, v117
	v_pk_mul_f32 v[116:117], v[130:131], v[130:131]
	v_pk_mul_f32 v[118:119], v[118:119], v[118:119]
	v_pk_fma_f32 v[116:117], v[128:129], v[128:129], v[116:117]
	v_pk_fma_f32 v[118:119], v[132:133], v[132:133], v[118:119]
	s_nop 0
	v_pk_add_f32 v[116:117], v[116:117], v[118:119]
	s_nop 0
	v_add_f32_e32 v113, v113, v116
	v_add_f32_e32 v113, v113, v117

.LBB0_410:
	s_or_b64 exec, exec, s[8:9]
	v_or_b32_e32 v238, 16, v232
	v_ashrrev_i32_e32 v239, 31, v238
	v_lshlrev_b64 v[112:113], 6, v[238:239]
	v_lshl_add_u64 v[112:113], s[16:17], 0, v[112:113]
	global_load_dwordx4 v[128:131], v[112:113], off
	global_load_dwordx4 v[132:135], v[112:113], off offset:16
	v_mul_f32_e32 v112, v109, v109
	v_mul_f32_e32 v113, v111, v111
	s_waitcnt lgkmcnt(0)
	v_mul_f32_e32 v117, v105, v105
	v_mul_f32_e32 v118, v107, v107
	v_fmac_f32_e32 v112, v108, v108
	v_fmac_f32_e32 v113, v110, v110
	v_fmac_f32_e32 v117, v104, v104
	v_fmac_f32_e32 v118, v106, v106
	v_cndmask_b32_e64 v119, 0, 1, s[62:63]
	v_add_f32_e32 v112, v112, v113
	v_add_f32_e32 v113, v117, v118
	v_cmp_ne_u32_e64 s[8:9], 1, v119
	v_add_f32_e32 v112, v112, v113
	s_mov_b64 s[26:27], -1
	s_waitcnt vmcnt(1)
	v_add_f32_e32 v128, v128, v129
	v_add_f32_e32 v129, v130, v131
	s_waitcnt vmcnt(0)
	v_add_f32_e32 v130, v132, v133
	v_add_f32_e32 v131, v134, v135
	v_add_f32_e32 v128, v128, v129
	v_add_f32_e32 v129, v130, v131
	v_add_f32_e32 v128, v128, v129
	v_fmamk_f32 v128, v128, 0x3b000000, v213
	v_rsq_f32_e32 v132, v128
	s_andn2_b64 vcc, exec, s[62:63]
	v_mul_f32_e32 v113, v132, v132
	s_cbranch_vccnz .LBB0_414
	s_and_b64 vcc, exec, s[6:7]
	v_mul_f32_e32 v117, v112, v113
	s_cbranch_vccnz .LBB0_413
	v_mov_b64_e32 v[118:119], s[50:51]
	v_mad_i64_i32 v[118:119], s[14:15], v238, s65, v[118:119]
	v_lshl_add_u64 v[118:119], v[208:209], 1, v[118:119]
	global_load_dwordx2 v[128:129], v[118:119], off offset:2080
	s_nop 0
	global_load_dwordx2 v[118:119], v[118:119], off offset:2048
	s_waitcnt vmcnt(1)
	v_lshlrev_b32_e32 v131, 16, v128
	v_and_b32_e32 v135, 0xffff0000, v128
	s_waitcnt vmcnt(0)
	v_and_b32_e32 v134, 0xffff0000, v118
	v_lshlrev_b32_e32 v137, 16, v129
	v_and_b32_e32 v129, 0xffff0000, v129
	v_and_b32_e32 v128, 0xffff0000, v119
	v_lshlrev_b32_e32 v130, 16, v118
	v_lshlrev_b32_e32 v136, 16, v119
	v_pk_mul_f32 v[118:119], v[134:135], v[134:135]
	v_pk_mul_f32 v[128:129], v[128:129], v[128:129]
	v_pk_fma_f32 v[118:119], v[130:131], v[130:131], v[118:119]
	v_pk_fma_f32 v[128:129], v[136:137], v[136:137], v[128:129]
	s_nop 0
	v_pk_add_f32 v[118:119], v[118:119], v[128:129]
	s_nop 0
	v_add_f32_e32 v117, v117, v118
	v_add_f32_e32 v117, v117, v119

.LBB0_420:
	s_or_b64 exec, exec, s[14:15]
	v_or_b32_e32 v228, 32, v232
	v_ashrrev_i32_e32 v229, 31, v228
	s_waitcnt lgkmcnt(0)
	v_lshlrev_b64 v[112:113], 6, v[228:229]
	v_lshl_add_u64 v[112:113], s[16:17], 0, v[112:113]
	global_load_dwordx4 v[128:131], v[112:113], off
	global_load_dwordx4 v[134:137], v[112:113], off offset:16
	v_mul_f32_e32 v112, v93, v93
	v_mul_f32_e32 v113, v95, v95
	v_mul_f32_e32 v117, v89, v89
	v_mul_f32_e32 v118, v91, v91
	v_fmac_f32_e32 v112, v92, v92
	v_fmac_f32_e32 v113, v94, v94
	v_fmac_f32_e32 v117, v88, v88
	v_fmac_f32_e32 v118, v90, v90
	v_add_f32_e32 v112, v112, v113
	v_add_f32_e32 v113, v117, v118
	v_add_f32_e32 v112, v112, v113
	s_mov_b64 s[26:27], -1
	s_waitcnt vmcnt(1)
	v_add_f32_e32 v119, v128, v129
	v_add_f32_e32 v128, v130, v131
	s_waitcnt vmcnt(0)
	v_add_f32_e32 v129, v134, v135
	v_add_f32_e32 v130, v136, v137
	v_add_f32_e32 v119, v119, v128
	v_add_f32_e32 v128, v129, v130
	v_add_f32_e32 v119, v119, v128
	v_fmamk_f32 v119, v119, 0x3b000000, v213
	v_rsq_f32_e32 v230, v119
	s_and_b64 vcc, exec, s[8:9]
	v_mul_f32_e32 v113, v230, v230
	s_cbranch_vccnz .LBB0_424
	s_and_b64 vcc, exec, s[6:7]
	v_mul_f32_e32 v117, v112, v113
	s_cbranch_vccnz .LBB0_423
	v_mov_b64_e32 v[118:119], s[50:51]
	v_mad_i64_i32 v[118:119], s[14:15], v228, s65, v[118:119]
	v_lshl_add_u64 v[118:119], v[208:209], 1, v[118:119]
	global_load_dwordx2 v[128:129], v[118:119], off offset:2080
	s_nop 0
	global_load_dwordx2 v[118:119], v[118:119], off offset:2048
	s_waitcnt vmcnt(1)
	v_lshlrev_b32_e32 v131, 16, v128
	v_and_b32_e32 v135, 0xffff0000, v128
	s_waitcnt vmcnt(0)
	v_and_b32_e32 v134, 0xffff0000, v118
	v_lshlrev_b32_e32 v137, 16, v129
	v_and_b32_e32 v129, 0xffff0000, v129
	v_and_b32_e32 v128, 0xffff0000, v119
	v_lshlrev_b32_e32 v130, 16, v118
	v_lshlrev_b32_e32 v136, 16, v119
	v_pk_mul_f32 v[118:119], v[134:135], v[134:135]
	v_pk_mul_f32 v[128:129], v[128:129], v[128:129]
	v_pk_fma_f32 v[118:119], v[130:131], v[130:131], v[118:119]
	v_pk_fma_f32 v[128:129], v[136:137], v[136:137], v[128:129]
	s_nop 0
	v_pk_add_f32 v[118:119], v[118:119], v[128:129]
	s_nop 0
	v_add_f32_e32 v117, v117, v118
	v_add_f32_e32 v117, v117, v119

.LBB0_430:
	s_or_b64 exec, exec, s[14:15]
	v_or_b32_e32 v234, 48, v232
	v_ashrrev_i32_e32 v235, 31, v234
	s_waitcnt lgkmcnt(0)
	v_lshlrev_b64 v[112:113], 6, v[234:235]
	v_lshl_add_u64 v[112:113], s[16:17], 0, v[112:113]
	global_load_dwordx4 v[128:131], v[112:113], off
	global_load_dwordx4 v[134:137], v[112:113], off offset:16
	v_mul_f32_e32 v112, v77, v77
	v_mul_f32_e32 v113, v79, v79
	v_mul_f32_e32 v117, v73, v73
	v_mul_f32_e32 v118, v75, v75
	v_fmac_f32_e32 v112, v76, v76
	v_fmac_f32_e32 v113, v78, v78
	v_fmac_f32_e32 v117, v72, v72
	v_fmac_f32_e32 v118, v74, v74
	v_add_f32_e32 v112, v112, v113
	v_add_f32_e32 v113, v117, v118
	v_add_f32_e32 v112, v112, v113
	s_mov_b64 s[26:27], -1
	s_waitcnt vmcnt(1)
	v_add_f32_e32 v119, v128, v129
	v_add_f32_e32 v128, v130, v131
	s_waitcnt vmcnt(0)
	v_add_f32_e32 v129, v134, v135
	v_add_f32_e32 v130, v136, v137
	v_add_f32_e32 v119, v119, v128
	v_add_f32_e32 v128, v129, v130
	v_add_f32_e32 v119, v119, v128
	v_fmamk_f32 v119, v119, 0x3b000000, v213
	v_rsq_f32_e32 v226, v119
	s_and_b64 vcc, exec, s[8:9]
	v_mul_f32_e32 v113, v226, v226
	s_cbranch_vccnz .LBB0_434
	s_and_b64 vcc, exec, s[6:7]
	v_mul_f32_e32 v117, v112, v113
	s_cbranch_vccnz .LBB0_433
	v_mov_b64_e32 v[118:119], s[50:51]
	v_mad_i64_i32 v[118:119], s[14:15], v234, s65, v[118:119]
	v_lshl_add_u64 v[118:119], v[208:209], 1, v[118:119]
	global_load_dwordx2 v[128:129], v[118:119], off offset:2080
	s_nop 0
	global_load_dwordx2 v[118:119], v[118:119], off offset:2048
	s_waitcnt vmcnt(1)
	v_lshlrev_b32_e32 v131, 16, v128
	v_and_b32_e32 v135, 0xffff0000, v128
	s_waitcnt vmcnt(0)
	v_and_b32_e32 v134, 0xffff0000, v118
	v_lshlrev_b32_e32 v137, 16, v129
	v_and_b32_e32 v129, 0xffff0000, v129
	v_and_b32_e32 v128, 0xffff0000, v119
	v_lshlrev_b32_e32 v130, 16, v118
	v_lshlrev_b32_e32 v136, 16, v119
	v_pk_mul_f32 v[118:119], v[134:135], v[134:135]
	v_pk_mul_f32 v[128:129], v[128:129], v[128:129]
	v_pk_fma_f32 v[118:119], v[130:131], v[130:131], v[118:119]
	v_pk_fma_f32 v[128:129], v[136:137], v[136:137], v[128:129]
	s_nop 0
	v_pk_add_f32 v[118:119], v[118:119], v[128:129]
	s_nop 0
	v_add_f32_e32 v117, v117, v118
	v_add_f32_e32 v117, v117, v119

.LBB0_440:
	s_or_b64 exec, exec, s[14:15]
	v_add_u32_e32 v112, 0x80, v232
	s_waitcnt lgkmcnt(0)
	v_ashrrev_i32_e32 v113, 31, v112
	v_lshlrev_b64 v[118:119], 6, v[112:113]
	v_lshl_add_u64 v[118:119], s[16:17], 0, v[118:119]
	global_load_dwordx4 v[128:131], v[118:119], off
	global_load_dwordx4 v[134:137], v[118:119], off offset:16
	v_mul_f32_e32 v113, v61, v61
	v_mul_f32_e32 v117, v63, v63
	v_mul_f32_e32 v118, v57, v57
	v_mul_f32_e32 v119, v59, v59
	v_fmac_f32_e32 v113, v60, v60
	v_fmac_f32_e32 v117, v62, v62
	v_fmac_f32_e32 v118, v56, v56
	v_fmac_f32_e32 v119, v58, v58
	v_add_f32_e32 v113, v113, v117
	v_add_f32_e32 v117, v118, v119
	v_add_f32_e32 v113, v113, v117
	s_mov_b64 s[26:27], -1
	s_waitcnt vmcnt(1)
	v_add_f32_e32 v128, v128, v129
	v_add_f32_e32 v129, v130, v131
	s_waitcnt vmcnt(0)
	v_add_f32_e32 v130, v134, v135
	v_add_f32_e32 v131, v136, v137
	v_add_f32_e32 v128, v128, v129
	v_add_f32_e32 v129, v130, v131
	v_add_f32_e32 v128, v128, v129
	v_fmamk_f32 v128, v128, 0x3b000000, v213
	v_rsq_f32_e32 v220, v128
	s_and_b64 vcc, exec, s[8:9]
	v_mul_f32_e32 v117, v220, v220
	s_cbranch_vccnz .LBB0_444
	s_and_b64 vcc, exec, s[6:7]
	v_mul_f32_e32 v118, v113, v117
	s_cbranch_vccnz .LBB0_443
	v_mov_b64_e32 v[128:129], s[50:51]
	v_mad_i64_i32 v[128:129], s[14:15], v112, s65, v[128:129]
	v_lshl_add_u64 v[128:129], v[208:209], 1, v[128:129]
	global_load_dwordx2 v[130:131], v[128:129], off offset:2080
	s_nop 0
	global_load_dwordx2 v[128:129], v[128:129], off offset:2048
	s_waitcnt vmcnt(1)
	v_lshlrev_b32_e32 v135, 16, v130
	v_and_b32_e32 v137, 0xffff0000, v130
	s_waitcnt vmcnt(0)
	v_and_b32_e32 v136, 0xffff0000, v128
	v_lshlrev_b32_e32 v139, 16, v131
	v_and_b32_e32 v131, 0xffff0000, v131
	v_and_b32_e32 v130, 0xffff0000, v129
	v_lshlrev_b32_e32 v134, 16, v128
	v_lshlrev_b32_e32 v138, 16, v129
	v_pk_mul_f32 v[128:129], v[136:137], v[136:137]
	v_pk_mul_f32 v[130:131], v[130:131], v[130:131]
	v_pk_fma_f32 v[128:129], v[134:135], v[134:135], v[128:129]
	v_pk_fma_f32 v[130:131], v[138:139], v[138:139], v[130:131]
	s_nop 0
	v_pk_add_f32 v[128:129], v[128:129], v[130:131]
	s_nop 0
	v_add_f32_e32 v112, v118, v128
	v_add_f32_e32 v118, v112, v129

.LBB0_450:
	s_or_b64 exec, exec, s[14:15]
	v_add_u32_e32 v112, 0x90, v232
	s_waitcnt lgkmcnt(0)
	v_ashrrev_i32_e32 v113, 31, v112
	v_lshlrev_b64 v[118:119], 6, v[112:113]
	v_lshl_add_u64 v[118:119], s[16:17], 0, v[118:119]
	global_load_dwordx4 v[128:131], v[118:119], off
	global_load_dwordx4 v[134:137], v[118:119], off offset:16
	v_mul_f32_e32 v113, v45, v45
	v_mul_f32_e32 v117, v47, v47
	v_mul_f32_e32 v118, v41, v41
	v_mul_f32_e32 v119, v43, v43
	v_fmac_f32_e32 v113, v44, v44
	v_fmac_f32_e32 v117, v46, v46
	v_fmac_f32_e32 v118, v40, v40
	v_fmac_f32_e32 v119, v42, v42
	v_add_f32_e32 v113, v113, v117
	v_add_f32_e32 v117, v118, v119
	v_add_f32_e32 v113, v113, v117
	s_mov_b64 s[26:27], -1
	s_waitcnt vmcnt(1)
	v_add_f32_e32 v128, v128, v129
	v_add_f32_e32 v129, v130, v131
	s_waitcnt vmcnt(0)
	v_add_f32_e32 v130, v134, v135
	v_add_f32_e32 v131, v136, v137
	v_add_f32_e32 v128, v128, v129
	v_add_f32_e32 v129, v130, v131
	v_add_f32_e32 v128, v128, v129
	v_fmamk_f32 v128, v128, 0x3b000000, v213
	v_rsq_f32_e32 v214, v128
	s_and_b64 vcc, exec, s[8:9]
	v_mul_f32_e32 v117, v214, v214
	s_cbranch_vccnz .LBB0_454
	s_and_b64 vcc, exec, s[6:7]
	v_mul_f32_e32 v118, v113, v117
	s_cbranch_vccnz .LBB0_453
	v_mov_b64_e32 v[128:129], s[50:51]
	v_mad_i64_i32 v[128:129], s[14:15], v112, s65, v[128:129]
	v_lshl_add_u64 v[128:129], v[208:209], 1, v[128:129]
	global_load_dwordx2 v[130:131], v[128:129], off offset:2080
	s_nop 0
	global_load_dwordx2 v[128:129], v[128:129], off offset:2048
	s_waitcnt vmcnt(1)
	v_lshlrev_b32_e32 v135, 16, v130
	v_and_b32_e32 v137, 0xffff0000, v130
	s_waitcnt vmcnt(0)
	v_and_b32_e32 v136, 0xffff0000, v128
	v_lshlrev_b32_e32 v139, 16, v131
	v_and_b32_e32 v131, 0xffff0000, v131
	v_and_b32_e32 v130, 0xffff0000, v129
	v_lshlrev_b32_e32 v134, 16, v128
	v_lshlrev_b32_e32 v138, 16, v129
	v_pk_mul_f32 v[128:129], v[136:137], v[136:137]
	v_pk_mul_f32 v[130:131], v[130:131], v[130:131]
	v_pk_fma_f32 v[128:129], v[134:135], v[134:135], v[128:129]
	v_pk_fma_f32 v[130:131], v[138:139], v[138:139], v[130:131]
	s_nop 0
	v_pk_add_f32 v[128:129], v[128:129], v[130:131]
	s_nop 0
	v_add_f32_e32 v112, v118, v128
	v_add_f32_e32 v118, v112, v129

.LBB0_460:
	s_or_b64 exec, exec, s[14:15]
	v_add_u32_e32 v112, 0xa0, v232
	s_waitcnt lgkmcnt(0)
	v_ashrrev_i32_e32 v113, 31, v112
	v_lshlrev_b64 v[118:119], 6, v[112:113]
	v_lshl_add_u64 v[118:119], s[16:17], 0, v[118:119]
	global_load_dwordx4 v[128:131], v[118:119], off
	global_load_dwordx4 v[134:137], v[118:119], off offset:16
	v_mul_f32_e32 v113, v29, v29
	v_mul_f32_e32 v117, v31, v31
	v_mul_f32_e32 v118, v25, v25
	v_mul_f32_e32 v119, v27, v27
	v_fmac_f32_e32 v113, v28, v28
	v_fmac_f32_e32 v117, v30, v30
	v_fmac_f32_e32 v118, v24, v24
	v_fmac_f32_e32 v119, v26, v26
	v_add_f32_e32 v113, v113, v117
	v_add_f32_e32 v117, v118, v119
	v_add_f32_e32 v113, v113, v117
	s_mov_b64 s[26:27], -1
	s_waitcnt vmcnt(1)
	v_add_f32_e32 v128, v128, v129
	v_add_f32_e32 v129, v130, v131
	s_waitcnt vmcnt(0)
	v_add_f32_e32 v130, v134, v135
	v_add_f32_e32 v131, v136, v137
	v_add_f32_e32 v128, v128, v129
	v_add_f32_e32 v129, v130, v131
	v_add_f32_e32 v128, v128, v129
	v_fmamk_f32 v128, v128, 0x3b000000, v213
	v_rsq_f32_e32 v212, v128
	s_and_b64 vcc, exec, s[8:9]
	v_mul_f32_e32 v117, v212, v212
	s_cbranch_vccnz .LBB0_464
	s_and_b64 vcc, exec, s[6:7]
	v_mul_f32_e32 v118, v113, v117
	s_cbranch_vccnz .LBB0_463
	v_mov_b64_e32 v[128:129], s[50:51]
	v_mad_i64_i32 v[128:129], s[14:15], v112, s65, v[128:129]
	v_lshl_add_u64 v[128:129], v[208:209], 1, v[128:129]
	global_load_dwordx2 v[130:131], v[128:129], off offset:2080
	s_nop 0
	global_load_dwordx2 v[128:129], v[128:129], off offset:2048
	s_waitcnt vmcnt(1)
	v_lshlrev_b32_e32 v135, 16, v130
	v_and_b32_e32 v137, 0xffff0000, v130
	s_waitcnt vmcnt(0)
	v_and_b32_e32 v136, 0xffff0000, v128
	v_lshlrev_b32_e32 v139, 16, v131
	v_and_b32_e32 v131, 0xffff0000, v131
	v_and_b32_e32 v130, 0xffff0000, v129
	v_lshlrev_b32_e32 v134, 16, v128
	v_lshlrev_b32_e32 v138, 16, v129
	v_pk_mul_f32 v[128:129], v[136:137], v[136:137]
	v_pk_mul_f32 v[130:131], v[130:131], v[130:131]
	v_pk_fma_f32 v[128:129], v[134:135], v[134:135], v[128:129]
	v_pk_fma_f32 v[130:131], v[138:139], v[138:139], v[130:131]
	s_nop 0
	v_pk_add_f32 v[128:129], v[128:129], v[130:131]
	s_nop 0
	v_add_f32_e32 v112, v118, v128
	v_add_f32_e32 v118, v112, v129

.LBB0_470:
	s_or_b64 exec, exec, s[14:15]
	v_add_u32_e32 v112, 0xb0, v232
	s_waitcnt lgkmcnt(0)
	v_ashrrev_i32_e32 v113, 31, v112
	v_lshlrev_b64 v[116:117], 6, v[112:113]
	v_lshl_add_u64 v[128:129], s[16:17], 0, v[116:117]
	global_load_dwordx4 v[116:119], v[128:129], off
	s_nop 0
	global_load_dwordx4 v[128:131], v[128:129], off offset:16
	v_mul_f32_e32 v113, v13, v13
	v_mul_f32_e32 v133, v15, v15
	v_mul_f32_e32 v134, v9, v9
	v_mul_f32_e32 v135, v11, v11
	v_fmac_f32_e32 v113, v12, v12
	v_fmac_f32_e32 v133, v14, v14
	v_fmac_f32_e32 v134, v8, v8
	v_fmac_f32_e32 v135, v10, v10
	v_add_f32_e32 v113, v113, v133
	s_mov_b64 s[14:15], -1
	s_waitcnt vmcnt(1)
	v_add_f32_e32 v116, v116, v117
	v_add_f32_e32 v117, v118, v119
	s_waitcnt vmcnt(0)
	v_add_f32_e32 v118, v128, v129
	v_add_f32_e32 v119, v130, v131
	v_add_f32_e32 v116, v116, v117
	v_add_f32_e32 v117, v118, v119
	v_add_f32_e32 v116, v116, v117
	v_fmamk_f32 v116, v116, 0x3b000000, v213
	v_rsq_f32_e32 v210, v116
	v_add_f32_e32 v118, v134, v135
	v_add_f32_e32 v113, v113, v118
	s_and_b64 vcc, exec, s[8:9]
	v_mul_f32_e32 v116, v210, v210
	s_cbranch_vccnz .LBB0_474
	s_and_b64 vcc, exec, s[6:7]
	v_mul_f32_e32 v117, v113, v116
	s_cbranch_vccnz .LBB0_473
	v_mov_b64_e32 v[118:119], s[50:51]
	v_mad_i64_i32 v[118:119], s[12:13], v112, s65, v[118:119]
	v_lshl_add_u64 v[118:119], v[208:209], 1, v[118:119]
	global_load_dwordx2 v[128:129], v[118:119], off offset:2080
	s_nop 0
	global_load_dwordx2 v[118:119], v[118:119], off offset:2048
	s_waitcnt vmcnt(1)
	v_lshlrev_b32_e32 v131, 16, v128
	v_and_b32_e32 v135, 0xffff0000, v128
	s_waitcnt vmcnt(0)
	v_and_b32_e32 v134, 0xffff0000, v118
	v_lshlrev_b32_e32 v137, 16, v129
	v_and_b32_e32 v129, 0xffff0000, v129
	v_and_b32_e32 v128, 0xffff0000, v119
	v_lshlrev_b32_e32 v130, 16, v118
	v_lshlrev_b32_e32 v136, 16, v119
	v_pk_mul_f32 v[118:119], v[134:135], v[134:135]
	v_pk_mul_f32 v[128:129], v[128:129], v[128:129]
	v_pk_fma_f32 v[118:119], v[130:131], v[130:131], v[118:119]
	v_pk_fma_f32 v[128:129], v[136:137], v[136:137], v[128:129]
	s_nop 0
	v_pk_add_f32 v[118:119], v[118:119], v[128:129]
	s_nop 0
	v_add_f32_e32 v112, v117, v118
	v_add_f32_e32 v117, v112, v119

.LBB0_494:
	s_or_b64 exec, exec, s[10:11]
	s_waitcnt lgkmcnt(7)
	v_add_f32_e32 v194, v194, v195
	v_add_f32_e32 v195, v196, v197
	v_add_f32_e32 v194, v194, v195
	v_fmamk_f32 v194, v194, 0x3baaaaab, v213
	v_rsq_f32_e32 v206, v194
	s_mul_i32 s58, s49, 0xc0
	s_lshl_b32 s26, s49, 7
	s_ashr_i32 s59, s58, 31
	s_ashr_i32 s27, s26, 31
	s_and_b64 s[10:11], s[16:17], exec
	s_nop 0
	s_mov_b32 s10, 0x30680000
	s_cselect_b32 s10, s10, 0x2d380000
	s_add_u32 s60, s18, s10
	s_addc_u32 s61, s19, 0
	v_mul_f32_e32 v196, v236, v206
	v_mov_b64_e32 v[194:195], s[60:61]
	v_mad_i64_i32 v[194:195], s[10:11], v232, s91, v[194:195]
	v_pk_mul_f32 v[152:153], v[152:153], v[196:197] op_sel_hi:[1,0]
	v_pk_mul_f32 v[154:155], v[154:155], v[196:197] op_sel_hi:[1,0]
	v_lshl_add_u64 v[194:195], s[58:59], 1, v[194:195]
	s_waitcnt vmcnt(0)
	v_pk_mul_f32 v[154:155], v[154:155], v[142:143]
	v_pk_mul_f32 v[152:153], v[152:153], v[140:141]
	v_lshl_add_u64 v[194:195], v[194:195], 0, s[34:35]
	v_pk_mul_f32 v[156:157], v[156:157], v[196:197] op_sel_hi:[1,0]
	v_cvt_pk_bf16_f32 v152, v152, v153
	v_cvt_pk_bf16_f32 v153, v154, v155
	v_cndmask_b32_e64 v154, 0, 1, s[16:17]
	v_lshl_add_u64 v[194:195], v[208:209], 1, v[194:195]
	v_pk_mul_f32 v[158:159], v[158:159], v[196:197] op_sel_hi:[1,0]
	v_pk_mul_f32 v[156:157], v[136:137], v[156:157]
	v_cmp_ne_u32_e64 s[10:11], 1, v154
	s_andn2_b64 vcc, exec, s[16:17]
	v_pk_mul_f32 v[158:159], v[138:139], v[158:159]
	v_cvt_pk_bf16_f32 v156, v156, v157
	global_store_dwordx2 v[194:195], v[152:153], off offset:32
	v_cvt_pk_bf16_f32 v157, v158, v159
	global_store_dwordx2 v[194:195], v[156:157], off
	s_cbranch_vccnz .LBB0_496
	v_lshlrev_b64 v[152:153], 11, v[232:233]
	v_lshl_add_u64 v[152:153], s[40:41], 0, v[152:153]
	v_lshl_add_u64 v[152:153], s[26:27], 1, v[152:153]
	v_lshl_add_u64 v[152:153], v[152:153], 0, s[34:35]
	v_pk_mul_f32 v[156:157], v[124:125], v[236:237] op_sel_hi:[1,0]
	v_lshl_add_u64 v[152:153], v[208:209], 1, v[152:153]
	v_pk_mul_f32 v[154:155], v[126:127], v[236:237] op_sel_hi:[1,0]
	v_cvt_pk_bf16_f32 v156, v156, v157
	s_nop 0
	v_cvt_pk_bf16_f32 v157, v154, v155
	global_store_dwordx2 v[152:153], v[156:157], off
	v_pk_mul_f32 v[156:157], v[120:121], v[236:237] op_sel_hi:[1,0]
	v_pk_mul_f32 v[154:155], v[122:123], v[236:237] op_sel_hi:[1,0]
	v_cvt_pk_bf16_f32 v156, v156, v157
	s_nop 0
	v_cvt_pk_bf16_f32 v157, v154, v155
	global_store_dwordx2 v[152:153], v[156:157], off offset:32

.LBB0_506:
	s_or_b64 exec, exec, s[16:17]
	s_waitcnt lgkmcnt(6)
	v_add_f32_e32 v120, v190, v191
	v_add_f32_e32 v121, v192, v193
	v_add_f32_e32 v120, v120, v121
	v_fmamk_f32 v120, v120, 0x3baaaaab, v213
	v_rsq_f32_e32 v126, v120
	v_add3_u32 v122, s48, v231, 16
	v_mov_b64_e32 v[120:121], s[60:61]
	v_mad_i64_i32 v[120:121], s[16:17], v122, s91, v[120:121]
	v_mul_f32_e32 v124, v132, v126
	v_lshl_add_u64 v[120:121], s[58:59], 1, v[120:121]
	v_lshl_add_u64 v[120:121], v[120:121], 0, s[34:35]
	v_pk_mul_f32 v[108:109], v[108:109], v[124:125] op_sel_hi:[1,0]
	v_pk_mul_f32 v[104:105], v[104:105], v[124:125] op_sel_hi:[1,0]
	v_ashrrev_i32_e32 v123, 31, v122
	v_lshl_add_u64 v[120:121], v[208:209], 1, v[120:121]
	v_pk_mul_f32 v[110:111], v[110:111], v[124:125] op_sel_hi:[1,0]
	v_pk_mul_f32 v[108:109], v[136:137], v[108:109]
	v_pk_mul_f32 v[106:107], v[106:107], v[124:125] op_sel_hi:[1,0]
	v_pk_mul_f32 v[104:105], v[104:105], v[140:141]
	s_and_b64 vcc, exec, s[10:11]
	v_pk_mul_f32 v[110:111], v[138:139], v[110:111]
	v_cvt_pk_bf16_f32 v108, v108, v109
	v_pk_mul_f32 v[106:107], v[106:107], v[142:143]
	v_cvt_pk_bf16_f32 v109, v110, v111
	global_store_dwordx2 v[120:121], v[108:109], off
	v_cvt_pk_bf16_f32 v104, v104, v105
	v_cvt_pk_bf16_f32 v105, v106, v107
	global_store_dwordx2 v[120:121], v[104:105], off offset:32
	s_cbranch_vccnz .LBB0_508
	v_lshlrev_b64 v[104:105], 11, v[122:123]
	v_lshl_add_u64 v[104:105], s[40:41], 0, v[104:105]
	v_lshl_add_u64 v[104:105], s[26:27], 1, v[104:105]
	v_lshl_add_u64 v[104:105], v[104:105], 0, s[34:35]
	v_pk_mul_f32 v[108:109], v[100:101], v[132:133] op_sel_hi:[1,0]
	v_lshl_add_u64 v[104:105], v[208:209], 1, v[104:105]
	v_pk_mul_f32 v[106:107], v[102:103], v[132:133] op_sel_hi:[1,0]
	v_cvt_pk_bf16_f32 v108, v108, v109
	s_nop 0
	v_cvt_pk_bf16_f32 v109, v106, v107
	global_store_dwordx2 v[104:105], v[108:109], off
	v_pk_mul_f32 v[108:109], v[96:97], v[132:133] op_sel_hi:[1,0]
	v_pk_mul_f32 v[106:107], v[98:99], v[132:133] op_sel_hi:[1,0]
	v_cvt_pk_bf16_f32 v108, v108, v109
	s_nop 0
	v_cvt_pk_bf16_f32 v109, v106, v107
	global_store_dwordx2 v[104:105], v[108:109], off offset:32

.LBB0_518:
	s_or_b64 exec, exec, s[16:17]
	s_waitcnt lgkmcnt(5)
	v_add_f32_e32 v96, v186, v187
	v_add_f32_e32 v97, v188, v189
	v_add_f32_e32 v96, v96, v97
	v_fmamk_f32 v96, v96, 0x3baaaaab, v213
	v_rsq_f32_e32 v100, v96
	v_mov_b64_e32 v[96:97], s[60:61]
	v_mad_i64_i32 v[96:97], s[16:17], v228, s91, v[96:97]
	v_mul_f32_e32 v98, v230, v100
	v_lshl_add_u64 v[96:97], s[58:59], 1, v[96:97]
	v_lshl_add_u64 v[96:97], v[96:97], 0, s[34:35]
	v_pk_mul_f32 v[92:93], v[92:93], v[98:99] op_sel_hi:[1,0]
	v_pk_mul_f32 v[88:89], v[88:89], v[98:99] op_sel_hi:[1,0]
	v_lshl_add_u64 v[96:97], v[208:209], 1, v[96:97]
	v_pk_mul_f32 v[94:95], v[94:95], v[98:99] op_sel_hi:[1,0]
	v_pk_mul_f32 v[92:93], v[136:137], v[92:93]
	v_pk_mul_f32 v[90:91], v[90:91], v[98:99] op_sel_hi:[1,0]
	v_pk_mul_f32 v[88:89], v[88:89], v[140:141]
	s_and_b64 vcc, exec, s[10:11]
	v_pk_mul_f32 v[94:95], v[138:139], v[94:95]
	v_cvt_pk_bf16_f32 v92, v92, v93
	v_pk_mul_f32 v[90:91], v[90:91], v[142:143]
	v_cvt_pk_bf16_f32 v93, v94, v95
	global_store_dwordx2 v[96:97], v[92:93], off
	v_cvt_pk_bf16_f32 v88, v88, v89
	v_cvt_pk_bf16_f32 v89, v90, v91
	global_store_dwordx2 v[96:97], v[88:89], off offset:32
	s_cbranch_vccnz .LBB0_520
	v_lshlrev_b64 v[88:89], 11, v[228:229]
	v_lshl_add_u64 v[88:89], s[40:41], 0, v[88:89]
	v_lshl_add_u64 v[88:89], s[26:27], 1, v[88:89]
	v_lshl_add_u64 v[88:89], v[88:89], 0, s[34:35]
	v_pk_mul_f32 v[92:93], v[84:85], v[230:231] op_sel_hi:[1,0]
	v_lshl_add_u64 v[88:89], v[208:209], 1, v[88:89]
	v_pk_mul_f32 v[90:91], v[86:87], v[230:231] op_sel_hi:[1,0]
	v_cvt_pk_bf16_f32 v92, v92, v93
	s_nop 0
	v_cvt_pk_bf16_f32 v93, v90, v91
	global_store_dwordx2 v[88:89], v[92:93], off
	v_pk_mul_f32 v[92:93], v[80:81], v[230:231] op_sel_hi:[1,0]
	v_pk_mul_f32 v[90:91], v[82:83], v[230:231] op_sel_hi:[1,0]
	v_cvt_pk_bf16_f32 v92, v92, v93
	s_nop 0
	v_cvt_pk_bf16_f32 v93, v90, v91
	global_store_dwordx2 v[88:89], v[92:93], off offset:32

.LBB0_532:
	s_or_b64 exec, exec, s[16:17]
	s_waitcnt lgkmcnt(4)
	v_add_f32_e32 v81, v182, v183
	v_add_f32_e32 v82, v184, v185
	v_add_f32_e32 v81, v81, v82
	v_fmamk_f32 v81, v81, 0x3baaaaab, v213
	v_rsq_f32_e32 v88, v81
	v_add3_u32 v84, s48, v231, 48
	v_mov_b64_e32 v[82:83], s[60:61]
	v_mad_i64_i32 v[82:83], s[16:17], v84, s91, v[82:83]
	v_mul_f32_e32 v86, v226, v88
	v_lshl_add_u64 v[82:83], s[58:59], 1, v[82:83]
	v_lshl_add_u64 v[82:83], v[82:83], 0, s[34:35]
	v_pk_mul_f32 v[76:77], v[76:77], v[86:87] op_sel_hi:[1,0]
	v_pk_mul_f32 v[72:73], v[72:73], v[86:87] op_sel_hi:[1,0]
	v_ashrrev_i32_e32 v85, 31, v84
	v_lshl_add_u64 v[82:83], v[208:209], 1, v[82:83]
	v_pk_mul_f32 v[78:79], v[78:79], v[86:87] op_sel_hi:[1,0]
	v_pk_mul_f32 v[76:77], v[136:137], v[76:77]
	v_pk_mul_f32 v[74:75], v[74:75], v[86:87] op_sel_hi:[1,0]
	v_pk_mul_f32 v[72:73], v[72:73], v[140:141]
	s_and_b64 vcc, exec, s[10:11]
	v_pk_mul_f32 v[78:79], v[138:139], v[78:79]
	v_cvt_pk_bf16_f32 v76, v76, v77
	v_pk_mul_f32 v[74:75], v[74:75], v[142:143]
	v_cvt_pk_bf16_f32 v77, v78, v79
	global_store_dwordx2 v[82:83], v[76:77], off
	v_cvt_pk_bf16_f32 v72, v72, v73
	v_cvt_pk_bf16_f32 v73, v74, v75
	global_store_dwordx2 v[82:83], v[72:73], off offset:32
	s_cbranch_vccnz .LBB0_534
	v_lshlrev_b64 v[72:73], 11, v[84:85]
	v_lshl_add_u64 v[72:73], s[40:41], 0, v[72:73]
	v_lshl_add_u64 v[72:73], s[26:27], 1, v[72:73]
	v_lshl_add_u64 v[72:73], v[72:73], 0, s[34:35]
	v_pk_mul_f32 v[76:77], v[68:69], v[226:227] op_sel_hi:[1,0]
	v_lshl_add_u64 v[72:73], v[208:209], 1, v[72:73]
	v_pk_mul_f32 v[74:75], v[70:71], v[226:227] op_sel_hi:[1,0]
	v_cvt_pk_bf16_f32 v76, v76, v77
	s_nop 0
	v_cvt_pk_bf16_f32 v77, v74, v75
	global_store_dwordx2 v[72:73], v[76:77], off
	v_pk_mul_f32 v[76:77], v[64:65], v[226:227] op_sel_hi:[1,0]
	v_pk_mul_f32 v[74:75], v[66:67], v[226:227] op_sel_hi:[1,0]
	v_cvt_pk_bf16_f32 v76, v76, v77
	s_nop 0
	v_cvt_pk_bf16_f32 v77, v74, v75
	global_store_dwordx2 v[72:73], v[76:77], off offset:32

.LBB0_546:
	s_or_b64 exec, exec, s[16:17]
	s_waitcnt lgkmcnt(3)
	v_add_f32_e32 v64, v178, v179
	v_add_f32_e32 v65, v180, v181
	v_add_f32_e32 v64, v64, v65
	v_fmamk_f32 v64, v64, 0x3baaaaab, v213
	v_rsq_f32_e32 v68, v64
	v_mov_b64_e32 v[64:65], s[60:61]
	v_mad_i64_i32 v[64:65], s[16:17], v80, s91, v[64:65]
	v_mul_f32_e32 v66, v220, v68
	v_lshl_add_u64 v[64:65], s[58:59], 1, v[64:65]
	v_lshl_add_u64 v[64:65], v[64:65], 0, s[34:35]
	v_pk_mul_f32 v[60:61], v[60:61], v[66:67] op_sel_hi:[1,0]
	v_pk_mul_f32 v[56:57], v[56:57], v[66:67] op_sel_hi:[1,0]
	v_lshl_add_u64 v[64:65], v[208:209], 1, v[64:65]
	v_pk_mul_f32 v[62:63], v[62:63], v[66:67] op_sel_hi:[1,0]
	v_pk_mul_f32 v[60:61], v[136:137], v[60:61]
	v_pk_mul_f32 v[58:59], v[58:59], v[66:67] op_sel_hi:[1,0]
	v_pk_mul_f32 v[56:57], v[56:57], v[140:141]
	s_and_b64 vcc, exec, s[10:11]
	v_pk_mul_f32 v[62:63], v[138:139], v[62:63]
	v_cvt_pk_bf16_f32 v60, v60, v61
	v_pk_mul_f32 v[58:59], v[58:59], v[142:143]
	v_cvt_pk_bf16_f32 v61, v62, v63
	global_store_dwordx2 v[64:65], v[60:61], off
	v_cvt_pk_bf16_f32 v56, v56, v57
	v_cvt_pk_bf16_f32 v57, v58, v59
	global_store_dwordx2 v[64:65], v[56:57], off offset:32
	s_cbranch_vccnz .LBB0_548
	v_ashrrev_i32_e32 v81, 31, v80
	v_lshlrev_b64 v[56:57], 11, v[80:81]
	v_lshl_add_u64 v[56:57], s[40:41], 0, v[56:57]
	v_lshl_add_u64 v[56:57], s[26:27], 1, v[56:57]
	v_lshl_add_u64 v[56:57], v[56:57], 0, s[34:35]
	v_pk_mul_f32 v[60:61], v[52:53], v[220:221] op_sel_hi:[1,0]
	v_lshl_add_u64 v[56:57], v[208:209], 1, v[56:57]
	v_pk_mul_f32 v[58:59], v[54:55], v[220:221] op_sel_hi:[1,0]
	v_cvt_pk_bf16_f32 v60, v60, v61
	s_nop 0
	v_cvt_pk_bf16_f32 v61, v58, v59
	global_store_dwordx2 v[56:57], v[60:61], off
	v_pk_mul_f32 v[60:61], v[48:49], v[220:221] op_sel_hi:[1,0]
	v_pk_mul_f32 v[58:59], v[50:51], v[220:221] op_sel_hi:[1,0]
	v_cvt_pk_bf16_f32 v60, v60, v61
	s_nop 0
	v_cvt_pk_bf16_f32 v61, v58, v59
	global_store_dwordx2 v[56:57], v[60:61], off offset:32

.LBB0_558:
	s_or_b64 exec, exec, s[16:17]
	s_waitcnt lgkmcnt(2)
	v_add_f32_e32 v49, v174, v175
	v_add_f32_e32 v50, v176, v177
	v_add_f32_e32 v49, v49, v50
	v_fmamk_f32 v49, v49, 0x3baaaaab, v213
	v_rsq_f32_e32 v56, v49
	v_add3_u32 v52, s48, v227, 16
	v_mov_b64_e32 v[50:51], s[60:61]
	v_mad_i64_i32 v[50:51], s[16:17], v52, s91, v[50:51]
	v_mul_f32_e32 v54, v214, v56
	v_lshl_add_u64 v[50:51], s[58:59], 1, v[50:51]
	v_lshl_add_u64 v[50:51], v[50:51], 0, s[34:35]
	v_pk_mul_f32 v[44:45], v[44:45], v[54:55] op_sel_hi:[1,0]
	v_pk_mul_f32 v[40:41], v[40:41], v[54:55] op_sel_hi:[1,0]
	v_ashrrev_i32_e32 v53, 31, v52
	v_lshl_add_u64 v[50:51], v[208:209], 1, v[50:51]
	v_pk_mul_f32 v[46:47], v[46:47], v[54:55] op_sel_hi:[1,0]
	v_pk_mul_f32 v[44:45], v[136:137], v[44:45]
	v_pk_mul_f32 v[42:43], v[42:43], v[54:55] op_sel_hi:[1,0]
	v_pk_mul_f32 v[40:41], v[40:41], v[140:141]
	s_and_b64 vcc, exec, s[10:11]
	v_pk_mul_f32 v[46:47], v[138:139], v[46:47]
	v_cvt_pk_bf16_f32 v44, v44, v45
	v_pk_mul_f32 v[42:43], v[42:43], v[142:143]
	v_cvt_pk_bf16_f32 v45, v46, v47
	global_store_dwordx2 v[50:51], v[44:45], off
	v_cvt_pk_bf16_f32 v40, v40, v41
	v_cvt_pk_bf16_f32 v41, v42, v43
	global_store_dwordx2 v[50:51], v[40:41], off offset:32
	s_cbranch_vccnz .LBB0_560
	v_lshlrev_b64 v[40:41], 11, v[52:53]
	v_lshl_add_u64 v[40:41], s[40:41], 0, v[40:41]
	v_lshl_add_u64 v[40:41], s[26:27], 1, v[40:41]
	v_lshl_add_u64 v[40:41], v[40:41], 0, s[34:35]
	v_pk_mul_f32 v[44:45], v[36:37], v[214:215] op_sel_hi:[1,0]
	v_lshl_add_u64 v[40:41], v[208:209], 1, v[40:41]
	v_pk_mul_f32 v[42:43], v[38:39], v[214:215] op_sel_hi:[1,0]
	v_cvt_pk_bf16_f32 v44, v44, v45
	s_nop 0
	v_cvt_pk_bf16_f32 v45, v42, v43
	global_store_dwordx2 v[40:41], v[44:45], off
	v_pk_mul_f32 v[44:45], v[32:33], v[214:215] op_sel_hi:[1,0]
	v_pk_mul_f32 v[42:43], v[34:35], v[214:215] op_sel_hi:[1,0]
	v_cvt_pk_bf16_f32 v44, v44, v45
	s_nop 0
	v_cvt_pk_bf16_f32 v45, v42, v43
	global_store_dwordx2 v[40:41], v[44:45], off offset:32

.LBB0_570:
	s_or_b64 exec, exec, s[12:13]
	s_waitcnt lgkmcnt(1)
	v_add_f32_e32 v32, v170, v171
	v_add_f32_e32 v33, v172, v173
	v_add_f32_e32 v32, v32, v33
	v_fmamk_f32 v32, v32, 0x3baaaaab, v213
	v_rsq_f32_e32 v36, v32
	v_mov_b64_e32 v[32:33], s[60:61]
	v_mad_i64_i32 v[32:33], s[12:13], v48, s91, v[32:33]
	v_mul_f32_e32 v34, v212, v36
	v_lshl_add_u64 v[32:33], s[58:59], 1, v[32:33]
	v_lshl_add_u64 v[32:33], v[32:33], 0, s[34:35]
	v_pk_mul_f32 v[28:29], v[28:29], v[34:35] op_sel_hi:[1,0]
	v_pk_mul_f32 v[24:25], v[24:25], v[34:35] op_sel_hi:[1,0]
	v_lshl_add_u64 v[32:33], v[208:209], 1, v[32:33]
	v_pk_mul_f32 v[30:31], v[30:31], v[34:35] op_sel_hi:[1,0]
	v_pk_mul_f32 v[28:29], v[136:137], v[28:29]
	v_pk_mul_f32 v[26:27], v[26:27], v[34:35] op_sel_hi:[1,0]
	v_pk_mul_f32 v[24:25], v[24:25], v[140:141]
	s_and_b64 vcc, exec, s[10:11]
	v_pk_mul_f32 v[30:31], v[138:139], v[30:31]
	v_cvt_pk_bf16_f32 v28, v28, v29
	v_pk_mul_f32 v[26:27], v[26:27], v[142:143]
	v_cvt_pk_bf16_f32 v29, v30, v31
	global_store_dwordx2 v[32:33], v[28:29], off
	v_cvt_pk_bf16_f32 v24, v24, v25
	v_cvt_pk_bf16_f32 v25, v26, v27
	global_store_dwordx2 v[32:33], v[24:25], off offset:32
	s_cbranch_vccnz .LBB0_572
	v_ashrrev_i32_e32 v49, 31, v48
	v_lshlrev_b64 v[24:25], 11, v[48:49]
	v_lshl_add_u64 v[24:25], s[40:41], 0, v[24:25]
	v_lshl_add_u64 v[24:25], s[26:27], 1, v[24:25]
	v_lshl_add_u64 v[24:25], v[24:25], 0, s[34:35]
	v_pk_mul_f32 v[28:29], v[20:21], v[212:213] op_sel_hi:[1,0]
	v_lshl_add_u64 v[24:25], v[208:209], 1, v[24:25]
	v_pk_mul_f32 v[26:27], v[22:23], v[212:213] op_sel_hi:[1,0]
	v_cvt_pk_bf16_f32 v28, v28, v29
	s_nop 0
	v_cvt_pk_bf16_f32 v29, v26, v27
	global_store_dwordx2 v[24:25], v[28:29], off
	v_pk_mul_f32 v[28:29], v[16:17], v[212:213] op_sel_hi:[1,0]
	v_pk_mul_f32 v[26:27], v[18:19], v[212:213] op_sel_hi:[1,0]
	v_cvt_pk_bf16_f32 v28, v28, v29
	s_nop 0
	v_cvt_pk_bf16_f32 v29, v26, v27
	global_store_dwordx2 v[24:25], v[28:29], off offset:32

.LBB0_580:
	s_waitcnt lgkmcnt(0)
	v_add_f32_e32 v16, v148, v149
	v_add_f32_e32 v17, v150, v151
	v_add_f32_e32 v16, v16, v17
	v_fmamk_f32 v16, v16, 0x3baaaaab, v213
	v_rsq_f32_e32 v22, v16
	v_add3_u32 v18, s48, v227, 48
	v_mov_b64_e32 v[16:17], s[60:61]
	v_mad_i64_i32 v[16:17], s[12:13], v18, s91, v[16:17]
	v_mul_f32_e32 v20, v210, v22
	v_lshl_add_u64 v[16:17], s[58:59], 1, v[16:17]
	v_lshl_add_u64 v[16:17], v[16:17], 0, s[34:35]
	v_pk_mul_f32 v[12:13], v[12:13], v[20:21] op_sel_hi:[1,0]
	v_pk_mul_f32 v[8:9], v[8:9], v[20:21] op_sel_hi:[1,0]
	v_ashrrev_i32_e32 v19, 31, v18
	v_lshl_add_u64 v[16:17], v[208:209], 1, v[16:17]
	v_pk_mul_f32 v[14:15], v[14:15], v[20:21] op_sel_hi:[1,0]
	v_pk_mul_f32 v[12:13], v[136:137], v[12:13]
	v_pk_mul_f32 v[10:11], v[10:11], v[20:21] op_sel_hi:[1,0]
	v_pk_mul_f32 v[8:9], v[8:9], v[140:141]
	s_and_b64 vcc, exec, s[10:11]
	v_pk_mul_f32 v[14:15], v[138:139], v[14:15]
	v_cvt_pk_bf16_f32 v12, v12, v13
	v_pk_mul_f32 v[10:11], v[10:11], v[142:143]
	v_cvt_pk_bf16_f32 v13, v14, v15
	global_store_dwordx2 v[16:17], v[12:13], off
	v_cvt_pk_bf16_f32 v8, v8, v9
	v_cvt_pk_bf16_f32 v9, v10, v11
	global_store_dwordx2 v[16:17], v[8:9], off offset:32
	s_cbranch_vccnz .LBB0_582
	v_lshlrev_b64 v[8:9], 11, v[18:19]
	v_lshl_add_u64 v[8:9], s[40:41], 0, v[8:9]
	v_lshl_add_u64 v[8:9], s[26:27], 1, v[8:9]
	v_lshl_add_u64 v[8:9], v[8:9], 0, s[34:35]
	v_pk_mul_f32 v[12:13], v[4:5], v[210:211] op_sel_hi:[1,0]
	v_lshl_add_u64 v[8:9], v[208:209], 1, v[8:9]
	v_pk_mul_f32 v[10:11], v[6:7], v[210:211] op_sel_hi:[1,0]
	v_cvt_pk_bf16_f32 v12, v12, v13
	s_nop 0
	v_cvt_pk_bf16_f32 v13, v10, v11
	global_store_dwordx2 v[8:9], v[12:13], off
	v_pk_mul_f32 v[12:13], v[0:1], v[210:211] op_sel_hi:[1,0]
	v_pk_mul_f32 v[10:11], v[2:3], v[210:211] op_sel_hi:[1,0]
	v_cvt_pk_bf16_f32 v12, v12, v13
	s_nop 0
	v_cvt_pk_bf16_f32 v13, v10, v11
	global_store_dwordx2 v[8:9], v[12:13], off offset:32
